# prologue main weight-copy loop: gating vmcnt waits, first uses and LDS address temps sunk below the last load of the 16-load batch
# speedup vs baseline: 1.0039x; 1.0000x over previous
.LBB0_67:
	s_andn2_b64 vcc, exec, s[38:39]
	s_cbranch_vccnz .LBB0_70
	s_cmpk_gt_u32 s80, 0x69f
	s_cbranch_scc1 .LBB0_70
	s_lshl_b32 s8, s40, 1
	s_and_b32 s30, s8, 0x1ff80
	s_lshl_b32 s8, s40, 5
	s_and_b32 s8, s8, 0x7e0
	v_or_b32_e32 v2, s8, v82
	v_or_b32_e32 v4, s30, v81
	v_lshlrev_b32_e32 v2, 2, v2
	v_mov_b32_e32 v3, v69
	v_lshl_add_u64 v[2:3], s[2:3], 0, v[2:3]
	v_lshlrev_b32_e32 v4, 13, v4
	v_mov_b32_e32 v5, v69
	v_lshl_add_u64 v[62:63], v[2:3], 0, v[4:5]
	v_add_co_u32_e32 v6, vcc, 0x10000, v62
	s_nop 1
	v_addc_co_u32_e32 v7, vcc, 0, v63, vcc
	global_load_dwordx4 v[2:5], v[62:63], off
	s_nop 0
	global_load_dwordx4 v[6:9], v[6:7], off
	v_add_co_u32_e32 v10, vcc, 0x20000, v62
	s_nop 0
	s_nop 0
	v_addc_co_u32_e32 v11, vcc, 0, v63, vcc
	v_add_co_u32_e32 v14, vcc, 0x30000, v62
	s_nop 1
	v_addc_co_u32_e32 v15, vcc, 0, v63, vcc
	global_load_dwordx4 v[10:13], v[10:11], off
	s_nop 0
	global_load_dwordx4 v[14:17], v[14:15], off
	v_add_co_u32_e32 v18, vcc, 0x40000, v62
	s_nop 1
	v_addc_co_u32_e32 v19, vcc, 0, v63, vcc
	v_add_co_u32_e32 v22, vcc, 0x50000, v62
	s_nop 1
	v_addc_co_u32_e32 v23, vcc, 0, v63, vcc
	global_load_dwordx4 v[18:21], v[18:19], off
	s_nop 0
	global_load_dwordx4 v[22:25], v[22:23], off
	v_add_co_u32_e32 v26, vcc, 0x60000, v62
	s_nop 0
	s_nop 0
	v_addc_co_u32_e32 v27, vcc, 0, v63, vcc
	global_load_dwordx4 v[26:29], v[26:27], off
	v_add_co_u32_e32 v30, vcc, 0x70000, v62
	s_nop 0
	s_nop 0
	v_addc_co_u32_e32 v31, vcc, 0, v63, vcc
	global_load_dwordx4 v[30:33], v[30:31], off
	v_add_co_u32_e32 v34, vcc, 0x80000, v62
	s_nop 0
	s_nop 0
	v_addc_co_u32_e32 v35, vcc, 0, v63, vcc
	global_load_dwordx4 v[34:37], v[34:35], off
	v_add_co_u32_e32 v38, vcc, 0x90000, v62
	s_nop 0
	s_nop 0
	v_addc_co_u32_e32 v39, vcc, 0, v63, vcc
	global_load_dwordx4 v[38:41], v[38:39], off
	v_add_co_u32_e32 v42, vcc, 0xa0000, v62
	s_nop 0
	s_nop 0
	v_addc_co_u32_e32 v43, vcc, 0, v63, vcc
	global_load_dwordx4 v[42:45], v[42:43], off
	v_add_co_u32_e32 v46, vcc, 0xb0000, v62
	s_nop 0
	s_nop 0
	v_addc_co_u32_e32 v47, vcc, 0, v63, vcc
	global_load_dwordx4 v[46:49], v[46:47], off
	v_add_co_u32_e32 v50, vcc, 0xc0000, v62
	s_nop 0
	s_nop 0
	v_addc_co_u32_e32 v51, vcc, 0, v63, vcc
	global_load_dwordx4 v[50:53], v[50:51], off
	v_add_co_u32_e32 v54, vcc, 0xd0000, v62
	s_nop 0
	s_nop 0
	v_addc_co_u32_e32 v55, vcc, 0, v63, vcc
	global_load_dwordx4 v[54:57], v[54:55], off
	v_add_co_u32_e32 v58, vcc, 0xe0000, v62
	s_nop 0
	s_nop 0
	v_addc_co_u32_e32 v59, vcc, 0, v63, vcc
	global_load_dwordx4 v[58:61], v[58:59], off
	v_add_co_u32_e32 v62, vcc, 0xf0000, v62
	s_nop 0
	s_nop 0
	v_addc_co_u32_e32 v63, vcc, 0, v63, vcc
	global_load_dwordx4 v[62:65], v[62:63], off
	s_waitcnt vmcnt(15)
	v_pk_mul_f32 v[2:3], v[2:3], s[34:35] op_sel_hi:[1,0]
	ds_write2_b32 v83, v2, v3 offset1:1
	v_pk_mul_f32 v[2:3], v[4:5], s[34:35] op_sel_hi:[1,0]
	ds_write2_b32 v83, v2, v3 offset0:2 offset1:3
	s_waitcnt vmcnt(14)
	v_pk_mul_f32 v[2:3], v[6:7], s[34:35] op_sel_hi:[1,0]
	ds_write2_b32 v89, v2, v3 offset1:1
	v_pk_mul_f32 v[2:3], v[8:9], s[34:35] op_sel_hi:[1,0]
	ds_write2_b32 v90, v2, v3 offset1:1
	v_add_u32_e32 v4, 0x2100, v83
	v_mov_b32_e32 v5, v69
	v_lshl_add_u64 v[6:7], v[72:73], 0, s[30:31]
	s_waitcnt vmcnt(13)
	v_pk_mul_f32 v[2:3], v[10:11], s[34:35] op_sel_hi:[1,0]
	ds_write2_b32 v91, v2, v3 offset1:1
	v_pk_mul_f32 v[2:3], v[12:13], s[34:35] op_sel_hi:[1,0]
	ds_write2_b32 v92, v2, v3 offset1:1
	s_waitcnt vmcnt(12)
	v_pk_mul_f32 v[2:3], v[14:15], s[34:35] op_sel_hi:[1,0]
	ds_write2_b32 v93, v2, v3 offset1:1
	v_pk_mul_f32 v[2:3], v[16:17], s[34:35] op_sel_hi:[1,0]
	ds_write2_b32 v94, v2, v3 offset1:1
	s_waitcnt vmcnt(11)
	v_pk_mul_f32 v[2:3], v[18:19], s[34:35] op_sel_hi:[1,0]
	ds_write2_b32 v95, v2, v3 offset1:1
	v_pk_mul_f32 v[2:3], v[20:21], s[34:35] op_sel_hi:[1,0]
	ds_write2_b32 v96, v2, v3 offset1:1
	s_waitcnt vmcnt(10)
	v_pk_mul_f32 v[2:3], v[22:23], s[34:35] op_sel_hi:[1,0]
	ds_write2_b32 v97, v2, v3 offset1:1
	v_pk_mul_f32 v[2:3], v[24:25], s[34:35] op_sel_hi:[1,0]
	ds_write2_b32 v98, v2, v3 offset1:1
	s_waitcnt vmcnt(9)
	v_pk_mul_f32 v[2:3], v[26:27], s[34:35] op_sel_hi:[1,0]
	ds_write2_b32 v99, v2, v3 offset1:1
	v_pk_mul_f32 v[2:3], v[28:29], s[34:35] op_sel_hi:[1,0]
	ds_write2_b32 v100, v2, v3 offset1:1
	s_waitcnt vmcnt(8)
	v_pk_mul_f32 v[2:3], v[30:31], s[34:35] op_sel_hi:[1,0]
	ds_write2_b32 v101, v2, v3 offset1:1
	v_pk_mul_f32 v[2:3], v[32:33], s[34:35] op_sel_hi:[1,0]
	ds_write2_b32 v102, v2, v3 offset1:1
	s_waitcnt vmcnt(7)
	v_pk_mul_f32 v[2:3], v[34:35], s[34:35] op_sel_hi:[1,0]
	ds_write2_b32 v4, v2, v3 offset1:1
	v_pk_mul_f32 v[2:3], v[36:37], s[34:35] op_sel_hi:[1,0]
	v_add_u32_e32 v4, 0x2108, v83
	ds_write2_b32 v4, v2, v3 offset1:1
	v_add_u32_e32 v4, 0x2520, v83
	s_waitcnt vmcnt(6)
	v_pk_mul_f32 v[2:3], v[38:39], s[34:35] op_sel_hi:[1,0]
	ds_write2_b32 v4, v2, v3 offset1:1
	v_pk_mul_f32 v[2:3], v[40:41], s[34:35] op_sel_hi:[1,0]
	v_add_u32_e32 v4, 0x2528, v83
	ds_write2_b32 v4, v2, v3 offset1:1
	v_add_u32_e32 v4, 0x2940, v83
	s_waitcnt vmcnt(5)
	v_pk_mul_f32 v[2:3], v[42:43], s[34:35] op_sel_hi:[1,0]
	ds_write2_b32 v4, v2, v3 offset1:1
	v_pk_mul_f32 v[2:3], v[44:45], s[34:35] op_sel_hi:[1,0]
	v_add_u32_e32 v4, 0x2948, v83
	ds_write2_b32 v4, v2, v3 offset1:1
	v_add_u32_e32 v4, 0x2d60, v83
	s_waitcnt vmcnt(4)
	v_pk_mul_f32 v[2:3], v[46:47], s[34:35] op_sel_hi:[1,0]
	ds_write2_b32 v4, v2, v3 offset1:1
	v_pk_mul_f32 v[2:3], v[48:49], s[34:35] op_sel_hi:[1,0]
	v_add_u32_e32 v4, 0x2d68, v83
	ds_write2_b32 v4, v2, v3 offset1:1
	v_add_u32_e32 v4, 0x3180, v83
	s_waitcnt vmcnt(3)
	v_pk_mul_f32 v[2:3], v[50:51], s[34:35] op_sel_hi:[1,0]
	ds_write2_b32 v4, v2, v3 offset1:1
	v_pk_mul_f32 v[2:3], v[52:53], s[34:35] op_sel_hi:[1,0]
	v_add_u32_e32 v4, 0x3188, v83
	ds_write2_b32 v4, v2, v3 offset1:1
	v_add_u32_e32 v4, 0x35a0, v83
	s_waitcnt vmcnt(2)
	v_pk_mul_f32 v[2:3], v[54:55], s[34:35] op_sel_hi:[1,0]
	ds_write2_b32 v4, v2, v3 offset1:1
	v_pk_mul_f32 v[2:3], v[56:57], s[34:35] op_sel_hi:[1,0]
	v_add_u32_e32 v4, 0x35a8, v83
	ds_write2_b32 v4, v2, v3 offset1:1
	v_add_u32_e32 v4, 0x39c0, v83
	s_waitcnt vmcnt(1)
	v_pk_mul_f32 v[2:3], v[58:59], s[34:35] op_sel_hi:[1,0]
	ds_write2_b32 v4, v2, v3 offset1:1
	v_pk_mul_f32 v[2:3], v[60:61], s[34:35] op_sel_hi:[1,0]
	v_add_u32_e32 v4, 0x39c8, v83
	ds_write2_b32 v4, v2, v3 offset1:1
	v_add_u32_e32 v4, 0x3de0, v83
	s_waitcnt vmcnt(0)
	v_pk_mul_f32 v[2:3], v[62:63], s[34:35] op_sel_hi:[1,0]
	ds_write2_b32 v4, v2, v3 offset1:1
	v_pk_mul_f32 v[2:3], v[64:65], s[34:35] op_sel_hi:[1,0]
	v_add_u32_e32 v4, 0x3de8, v83
	ds_write2_b32 v4, v2, v3 offset1:1
	s_waitcnt lgkmcnt(0)
	v_add_u32_e32 v42, 0x400, v88
	ds_read2_b32 v[8:9], v42 offset0:206 offset1:214
	ds_read2_b32 v[10:11], v42 offset0:239 offset1:247
	ds_read2_b32 v[12:13], v42 offset0:140 offset1:148
	ds_read2_b32 v[14:15], v42 offset0:173 offset1:181
	ds_read2_b32 v[16:17], v42 offset0:74 offset1:82
	ds_read2_b32 v[18:19], v42 offset0:107 offset1:115
	ds_read2_b32 v[20:21], v42 offset0:8 offset1:16
	ds_read2_b32 v[22:23], v42 offset0:41 offset1:49
	s_waitcnt lgkmcnt(7)
	v_med3_f32 v2, v8, s53, v103
	s_waitcnt lgkmcnt(6)
	v_med3_f32 v3, v10, s53, v103
	s_waitcnt lgkmcnt(5)
	v_med3_f32 v4, v12, s53, v103
	s_waitcnt lgkmcnt(4)
	v_med3_f32 v8, v14, s53, v103
	v_cvt_pk_fp8_f32 v5, v4, v8
	s_waitcnt lgkmcnt(1)
	v_med3_f32 v8, v20, s53, v103
	s_waitcnt lgkmcnt(0)
	v_med3_f32 v10, v22, s53, v103
	v_mov_b32_e32 v4, v69
	ds_read2_b32 v[24:25], v88 offset0:198 offset1:206
	ds_read2_b32 v[26:27], v88 offset0:231 offset1:239
	ds_read2_b32 v[28:29], v88 offset0:132 offset1:140
	ds_read2_b32 v[30:31], v88 offset0:165 offset1:173
	v_cvt_pk_fp8_f32 v4, v8, v10
	ds_read2_b32 v[32:33], v88 offset1:8
	ds_read2_b32 v[34:35], v88 offset0:33 offset1:41
	v_cvt_pk_fp8_f32 v5, v2, v3 op_sel:[0,0,1]
	v_med3_f32 v2, v16, s53, v103
	v_med3_f32 v3, v18, s53, v103
	v_cvt_pk_fp8_f32 v4, v2, v3 op_sel:[0,0,1]
	s_waitcnt lgkmcnt(3)
	v_med3_f32 v2, v28, s53, v103
	s_waitcnt lgkmcnt(2)
	v_med3_f32 v12, v30, s53, v103
	v_mov_b32_e32 v3, v69
	ds_read2_b32 v[36:37], v88 offset0:66 offset1:74
	ds_read2_b32 v[38:39], v88 offset0:99 offset1:107
	v_cvt_pk_fp8_f32 v3, v2, v12
	s_waitcnt lgkmcnt(3)
	v_med3_f32 v12, v32, s53, v103
	s_waitcnt lgkmcnt(2)
	v_med3_f32 v14, v34, s53, v103
	v_mov_b32_e32 v2, v69
	v_cvt_pk_fp8_f32 v2, v12, v14
	v_med3_f32 v8, v24, s53, v103
	v_med3_f32 v10, v26, s53, v103
	v_cvt_pk_fp8_f32 v3, v8, v10 op_sel:[0,0,1]
	s_waitcnt lgkmcnt(1)
	v_med3_f32 v8, v36, s53, v103
	s_waitcnt lgkmcnt(0)
	v_med3_f32 v10, v38, s53, v103
	v_cvt_pk_fp8_f32 v2, v8, v10 op_sel:[0,0,1]
	v_or_b32_e32 v40, s8, v81
	v_lshlrev_b32_e32 v40, 11, v40
	v_mov_b32_e32 v41, v69
	v_lshl_add_u64 v[40:41], v[6:7], 0, v[40:41]
	global_store_dwordx4 v[40:41], v[2:5], off
	v_med3_f32 v10, v23, s53, v103
	v_med3_f32 v12, v35, s53, v103
	v_med3_f32 v2, v9, s53, v103
	v_med3_f32 v4, v13, s53, v103
	v_med3_f32 v9, v15, s53, v103
	v_mov_b32_e32 v5, v69
	v_cvt_pk_fp8_f32 v5, v4, v9
	v_med3_f32 v9, v21, s53, v103
	v_mov_b32_e32 v4, v69
	v_cvt_pk_fp8_f32 v4, v9, v10
	v_med3_f32 v3, v11, s53, v103
	v_cvt_pk_fp8_f32 v5, v2, v3 op_sel:[0,0,1]
	v_med3_f32 v2, v17, s53, v103
	v_med3_f32 v3, v19, s53, v103
	v_cvt_pk_fp8_f32 v4, v2, v3 op_sel:[0,0,1]
	v_med3_f32 v2, v29, s53, v103
	v_med3_f32 v11, v31, s53, v103
	v_mov_b32_e32 v3, v69
	v_cvt_pk_fp8_f32 v3, v2, v11
	v_med3_f32 v11, v33, s53, v103
	v_mov_b32_e32 v2, v69
	v_cvt_pk_fp8_f32 v2, v11, v12
	v_med3_f32 v9, v25, s53, v103
	v_med3_f32 v10, v27, s53, v103
	v_cvt_pk_fp8_f32 v3, v9, v10 op_sel:[0,0,1]
	v_med3_f32 v9, v37, s53, v103
	v_med3_f32 v10, v39, s53, v103
	v_cvt_pk_fp8_f32 v2, v9, v10 op_sel:[0,0,1]
	v_or_b32_e32 v8, s8, v84
	v_lshlrev_b32_e32 v8, 11, v8
	v_mov_b32_e32 v9, v69
	v_lshl_add_u64 v[8:9], v[6:7], 0, v[8:9]
	global_store_dwordx4 v[8:9], v[2:5], off
	ds_read2_b32 v[8:9], v42 offset0:222 offset1:230
	v_or_b32_e32 v40, s8, v85
	v_add_u32_e32 v2, 0x600, v88
	ds_read2_b32 v[10:11], v2 offset0:127 offset1:135
	ds_read2_b32 v[12:13], v42 offset0:156 offset1:164
	ds_read2_b32 v[14:15], v42 offset0:189 offset1:197
	ds_read2_b32 v[16:17], v42 offset0:90 offset1:98
	ds_read2_b32 v[18:19], v42 offset0:123 offset1:131
	ds_read2_b32 v[20:21], v42 offset0:24 offset1:32
	ds_read2_b32 v[22:23], v42 offset0:57 offset1:65
	s_waitcnt lgkmcnt(7)
	v_med3_f32 v2, v8, s53, v103
	v_mov_b32_e32 v5, v69
	s_waitcnt lgkmcnt(5)
	v_med3_f32 v4, v12, s53, v103
	s_waitcnt lgkmcnt(4)
	v_med3_f32 v8, v14, s53, v103
	v_med3_f32 v3, v10, s53, v103
	v_cvt_pk_fp8_f32 v5, v4, v8
	s_waitcnt lgkmcnt(1)
	v_med3_f32 v8, v20, s53, v103
	s_waitcnt lgkmcnt(0)
	v_med3_f32 v10, v22, s53, v103
	v_mov_b32_e32 v4, v69
	ds_read2_b32 v[24:25], v88 offset0:214 offset1:222
	ds_read2_b32 v[26:27], v88 offset0:247 offset1:255
	ds_read2_b32 v[28:29], v88 offset0:148 offset1:156
	ds_read2_b32 v[30:31], v88 offset0:181 offset1:189
	v_cvt_pk_fp8_f32 v4, v8, v10
	ds_read2_b32 v[32:33], v88 offset0:16 offset1:24
	ds_read2_b32 v[34:35], v88 offset0:49 offset1:57
	v_cvt_pk_fp8_f32 v5, v2, v3 op_sel:[0,0,1]
	v_med3_f32 v2, v16, s53, v103
	v_med3_f32 v3, v18, s53, v103
	v_cvt_pk_fp8_f32 v4, v2, v3 op_sel:[0,0,1]
	s_waitcnt lgkmcnt(3)
	v_med3_f32 v2, v28, s53, v103
	s_waitcnt lgkmcnt(2)
	v_med3_f32 v12, v30, s53, v103
	v_mov_b32_e32 v3, v69
	ds_read2_b32 v[36:37], v88 offset0:82 offset1:90
	ds_read2_b32 v[38:39], v88 offset0:115 offset1:123
	v_cvt_pk_fp8_f32 v3, v2, v12
	s_waitcnt lgkmcnt(3)
	v_med3_f32 v12, v32, s53, v103
	s_waitcnt lgkmcnt(2)
	v_med3_f32 v14, v34, s53, v103
	v_mov_b32_e32 v2, v69
	v_cvt_pk_fp8_f32 v2, v12, v14
	v_med3_f32 v8, v24, s53, v103
	v_med3_f32 v10, v26, s53, v103
	v_cvt_pk_fp8_f32 v3, v8, v10 op_sel:[0,0,1]
	s_waitcnt lgkmcnt(1)
	v_med3_f32 v8, v36, s53, v103
	s_waitcnt lgkmcnt(0)
	v_med3_f32 v10, v38, s53, v103
	v_cvt_pk_fp8_f32 v2, v8, v10 op_sel:[0,0,1]
	v_lshlrev_b32_e32 v40, 11, v40
	v_mov_b32_e32 v41, v69
	v_lshl_add_u64 v[40:41], v[6:7], 0, v[40:41]
	global_store_dwordx4 v[40:41], v[2:5], off
	v_med3_f32 v10, v23, s53, v103
	v_med3_f32 v12, v35, s53, v103
	v_med3_f32 v2, v9, s53, v103
	v_med3_f32 v4, v13, s53, v103
	v_med3_f32 v9, v15, s53, v103
	v_mov_b32_e32 v5, v69
	v_cvt_pk_fp8_f32 v5, v4, v9
	v_med3_f32 v9, v21, s53, v103
	v_mov_b32_e32 v4, v69
	v_cvt_pk_fp8_f32 v4, v9, v10
	v_med3_f32 v3, v11, s53, v103
	v_cvt_pk_fp8_f32 v5, v2, v3 op_sel:[0,0,1]
	v_med3_f32 v2, v17, s53, v103
	v_med3_f32 v3, v19, s53, v103
	v_cvt_pk_fp8_f32 v4, v2, v3 op_sel:[0,0,1]
	v_med3_f32 v2, v29, s53, v103
	v_med3_f32 v11, v31, s53, v103
	v_mov_b32_e32 v3, v69
	v_cvt_pk_fp8_f32 v3, v2, v11
	v_med3_f32 v11, v33, s53, v103
	v_mov_b32_e32 v2, v69
	v_cvt_pk_fp8_f32 v2, v11, v12
	v_med3_f32 v9, v25, s53, v103
	v_med3_f32 v10, v27, s53, v103
	v_cvt_pk_fp8_f32 v3, v9, v10 op_sel:[0,0,1]
	v_med3_f32 v9, v37, s53, v103
	v_med3_f32 v10, v39, s53, v103
	v_cvt_pk_fp8_f32 v2, v9, v10 op_sel:[0,0,1]
	v_or_b32_e32 v8, s8, v86
	v_lshlrev_b32_e32 v8, 11, v8
	v_mov_b32_e32 v9, v69
	v_lshl_add_u64 v[6:7], v[6:7], 0, v[8:9]
	global_store_dwordx4 v[6:7], v[2:5], off
	s_waitcnt lgkmcnt(0)
